# speedup vs baseline: 1.0223x; 1.0223x over previous
.LBB1_19:
	s_andn2_saveexec_b64 s[14:15], s[14:15]
	s_cbranch_execz .LBB1_16
	v_add_u32_e32 v18, -10, v8
	v_cmp_gt_u32_e32 vcc, 4, v18
	s_nop 1
	v_cndmask_b32_e64 v18, 0, 6, vcc
	v_xor_b32_e32 v18, v8, v18
	v_mov_b32_e32 v19, 0
	v_lshl_add_u64 v[18:19], v[18:19], 1, v[22:23]
	v_lshl_add_u64 v[18:19], s[8:9], 0, v[18:19]
	global_store_short v[18:19], v17, off
	s_branch .LBB1_16
.LBB1_21:
	s_or_b64 exec, exec, s[4:5]
	s_lshr_b32 s4, s18, 16
	v_cvt_f32_u32_e32 v3, s4
	v_lshlrev_b64 v[8:9], 11, v[6:7]
	v_lshl_add_u64 v[8:9], s[16:17], 0, v[8:9]
	s_and_b32 s10, s18, 0xffff
	v_div_scale_f32 v4, s[4:5], v3, v3, 1.0
	v_rcp_f32_e32 v12, v4
	v_div_scale_f32 v13, vcc, 1.0, v3, 1.0
	v_readlane_b32 s4, v16, 0
	v_fma_f32 v17, -v4, v12, 1.0
	v_fmac_f32_e32 v12, v17, v12
	v_mul_f32_e32 v17, v13, v12
	v_fma_f32 v18, -v4, v17, v13
	v_fmac_f32_e32 v17, v18, v12
	v_fma_f32 v4, -v4, v17, v13
	v_div_fmas_f32 v4, v4, v12, v17
	v_readlane_b32 s5, v16, 1
	v_div_fixup_f32 v4, v4, v3, 1.0
	v_mov_b32_e32 v12, s4
	v_mov_b32_e32 v3, s5
	v_cmp_gt_u32_e32 vcc, 32, v2
	s_nop 1
	v_cndmask_b32_e32 v3, v3, v12, vcc
	v_and_b32_e32 v3, v3, v15
	v_cmp_ne_u32_e64 s[4:5], 0, v3
	v_mov_b32_e32 v3, 0
	v_lshl_add_u64 v[8:9], v[2:3], 2, v[8:9]
	v_cndmask_b32_e64 v12, 0, v4, s[4:5]
	v_readlane_b32 s4, v16, 2
	v_readlane_b32 s5, v16, 3
	global_store_dword v[8:9], v12, off
	v_mov_b32_e32 v13, s4
	v_mov_b32_e32 v12, s5
	v_cndmask_b32_e32 v12, v12, v13, vcc
	v_and_b32_e32 v12, v12, v15
	v_cmp_ne_u32_e64 s[4:5], 0, v12
	s_nop 1
	v_cndmask_b32_e64 v12, 0, v4, s[4:5]
	v_readlane_b32 s4, v16, 4
	v_readlane_b32 s5, v16, 5
	global_store_dword v[8:9], v12, off offset:256
	v_mov_b32_e32 v13, s4
	v_mov_b32_e32 v12, s5
	v_cndmask_b32_e32 v12, v12, v13, vcc
	v_and_b32_e32 v12, v12, v15
	v_cmp_ne_u32_e64 s[4:5], 0, v12
	s_nop 1
	v_cndmask_b32_e64 v12, 0, v4, s[4:5]
	v_readlane_b32 s4, v16, 6
	v_readlane_b32 s5, v16, 7
	global_store_dword v[8:9], v12, off offset:512
	v_mov_b32_e32 v13, s4
	v_mov_b32_e32 v12, s5
	v_cndmask_b32_e32 v12, v12, v13, vcc
	v_and_b32_e32 v12, v12, v15
	v_cmp_ne_u32_e64 s[4:5], 0, v12
	s_nop 1
	v_cndmask_b32_e64 v12, 0, v4, s[4:5]
	v_readlane_b32 s4, v16, 8
	v_readlane_b32 s5, v16, 9
	global_store_dword v[8:9], v12, off offset:768
	v_mov_b32_e32 v13, s4
	v_mov_b32_e32 v12, s5
	v_cndmask_b32_e32 v12, v12, v13, vcc
	v_and_b32_e32 v12, v12, v15
	v_cmp_ne_u32_e64 s[4:5], 0, v12
	s_nop 1
	v_cndmask_b32_e64 v12, 0, v4, s[4:5]
	v_readlane_b32 s4, v16, 10
	v_readlane_b32 s5, v16, 11
	global_store_dword v[8:9], v12, off offset:1024
	v_mov_b32_e32 v13, s4
	v_mov_b32_e32 v12, s5
	v_cndmask_b32_e32 v12, v12, v13, vcc
	v_and_b32_e32 v12, v12, v15
	v_cmp_ne_u32_e64 s[4:5], 0, v12
	s_nop 1
	v_cndmask_b32_e64 v12, 0, v4, s[4:5]
	v_readlane_b32 s4, v16, 12
	v_readlane_b32 s5, v16, 13
	global_store_dword v[8:9], v12, off offset:1280
	v_mov_b32_e32 v13, s4
	v_mov_b32_e32 v12, s5
	v_cndmask_b32_e32 v12, v12, v13, vcc
	v_and_b32_e32 v12, v12, v15
	v_cmp_ne_u32_e64 s[4:5], 0, v12
	s_nop 1
	v_cndmask_b32_e64 v12, 0, v4, s[4:5]
	v_readlane_b32 s4, v16, 14
	v_readlane_b32 s5, v16, 15
	global_store_dword v[8:9], v12, off offset:1536
	v_mov_b32_e32 v13, s4
	v_mov_b32_e32 v12, s5
	v_cndmask_b32_e32 v12, v12, v13, vcc
	v_and_b32_e32 v12, v12, v15
	v_cmp_ne_u32_e32 vcc, 0, v12
	v_cmp_le_u32_e64 s[4:5], s10, v2
	s_nop 0
	v_cndmask_b32_e32 v12, 0, v4, vcc
	v_cmp_gt_u32_e32 vcc, 24, v2
	s_and_b64 s[14:15], vcc, s[4:5]
	global_store_dword v[8:9], v12, off offset:1792
	s_and_saveexec_b64 s[4:5], s[14:15]
	s_cbranch_execz .LBB1_23
	v_mad_u64_u32 v[8:9], s[8:9], v6, 48, s[8:9]
	v_mad_u32_u24 v9, v7, 48, v9
	v_add_u32_e32 v12, -10, v2
	v_cmp_gt_u32_e32 vcc, 4, v12
	s_nop 1
	v_cndmask_b32_e64 v12, 0, 6, vcc
	v_xor_b32_e32 v12, v2, v12
	v_mov_b32_e32 v13, 0
	v_lshl_add_u64 v[8:9], v[12:13], 1, v[8:9]
	v_mov_b32_e32 v3, 0x2000
	global_store_short v[8:9], v3, off

_Z8k3_chainPKfPK15HIP_vector_typeIiLj4EEPKtS6_S0_S0_Pf:
	s_load_dwordx8 s[8:15], s[0:1], 0x0
	s_load_dwordx4 s[4:7], s[0:1], 0x20
	s_load_dwordx2 s[16:17], s[0:1], 0x30
	s_mul_hi_u32 s0, s2, 0xaaaaaaab
	s_lshr_b32 s20, s0, 5
	s_mul_i32 s0, s20, 48
	s_mov_b32 s21, 0
	s_sub_i32 s18, s2, s0
	s_lshl_b64 s[0:1], s[20:21], 13
	s_waitcnt lgkmcnt(0)
	s_add_u32 s2, s10, s0
	v_and_b32_e32 v1, 3, v0
	s_addc_u32 s3, s11, s1
	s_mul_hi_u32 s1, s20, 0x18000
	s_mul_i32 s0, s20, 0x18000
	v_lshlrev_b32_e32 v104, 4, v0
	v_mov_b32_e32 v105, 0
	v_lshl_or_b32 v98, s18, 2, v1
	s_lshl_b64 s[18:19], s[0:1], 4
	v_lshl_add_u64 v[2:3], s[2:3], 0, v[104:105]
	s_add_u32 s0, s8, s18
	s_movk_i32 s8, 0x1000
	v_add_co_u32_e32 v10, vcc, s8, v2
	s_addc_u32 s1, s9, s19
	s_nop 0
	v_addc_co_u32_e32 v11, vcc, 0, v3, vcc
	global_load_dwordx4 v[2:5], v104, s[2:3]
	global_load_dwordx4 v[6:9], v[10:11], off
	s_mul_i32 s2, s20, 0x6000
	s_mul_hi_u32 s3, s20, 0x6000
	s_add_u32 s2, s12, s2
	s_addc_u32 s3, s13, s3
	v_lshl_add_u64 v[10:11], s[2:3], 0, v[104:105]
	s_movk_i32 s8, 0x2000
	v_add_co_u32_e32 v12, vcc, s8, v10
	s_movk_i32 s8, 0x3000
	s_nop 0
	v_addc_co_u32_e32 v13, vcc, 0, v11, vcc
	global_load_dwordx4 v[38:41], v104, s[2:3]
	global_load_dwordx4 v[42:45], v[12:13], off offset:-4096
	global_load_dwordx4 v[46:49], v[12:13], off
	v_add_co_u32_e32 v12, vcc, s8, v10
	v_lshrrev_b32_e32 v110, 2, v0
	s_nop 0
	v_addc_co_u32_e32 v13, vcc, 0, v11, vcc
	v_or_b32_e32 v14, 0x4000, v104
	global_load_dwordx4 v[50:53], v[12:13], off
	global_load_dwordx4 v[54:57], v14, s[2:3]
	s_movk_i32 s2, 0x5000
	v_add_co_u32_e32 v10, vcc, s2, v10
	s_movk_i32 s2, 0xc0
	v_or_b32_e32 v18, 64, v110
	v_addc_co_u32_e32 v11, vcc, 0, v11, vcc
	v_mov_b32_e32 v99, v105
	v_mad_u32_u24 v106, v110, s2, v98
	v_mov_b32_e32 v107, v105
	v_mul_u32_u24_e32 v102, 0xc00, v18
	v_mov_b32_e32 v103, v105
	global_load_dwordx4 v[66:69], v[10:11], off
	v_lshlrev_b64 v[10:11], 4, v[106:107]
	v_lshl_add_u64 v[14:15], s[0:1], 0, v[102:103]
	v_lshlrev_b64 v[16:17], 4, v[98:99]
	v_lshl_add_u64 v[12:13], s[0:1], 0, v[10:11]
	v_lshl_add_u64 v[14:15], v[14:15], 0, v[16:17]
	s_mov_b32 s3, 0x30000
	global_load_dwordx4 v[58:61], v[12:13], off
	global_load_dwordx4 v[62:65], v[14:15], off
	v_add_co_u32_e32 v12, vcc, s3, v14
	s_mov_b32 s3, 0x60000
	s_nop 0
	v_addc_co_u32_e32 v13, vcc, 0, v15, vcc
	v_add_co_u32_e32 v14, vcc, s3, v14
	s_movk_i32 s2, 0xc00
	s_nop 0
	v_addc_co_u32_e32 v15, vcc, 0, v15, vcc
	global_load_dwordx4 v[70:73], v[12:13], off
	global_load_dwordx4 v[74:77], v[14:15], off
	v_mov_b32_e32 v12, 0x90000
	v_mad_u32_u24 v12, v18, s2, v12
	v_mov_b32_e32 v13, v105
	v_mov_b32_e32 v14, 0xc0000
	v_lshl_add_u64 v[12:13], s[0:1], 0, v[12:13]
	v_mad_u32_u24 v100, v18, s2, v14
	v_mov_b32_e32 v101, v105
	v_lshl_add_u64 v[12:13], v[12:13], 0, v[16:17]
	v_lshl_add_u64 v[14:15], s[0:1], 0, v[100:101]
	v_lshl_add_u64 v[14:15], v[14:15], 0, v[16:17]
	global_load_dwordx4 v[78:81], v[12:13], off
	global_load_dwordx4 v[82:85], v[14:15], off
	v_mov_b32_e32 v12, 0xf0000
	v_mad_u32_u24 v96, v18, s2, v12
	v_mov_b32_e32 v97, v105
	v_mov_b32_e32 v14, 0x120000
	v_lshl_add_u64 v[12:13], s[0:1], 0, v[96:97]
	v_mad_u32_u24 v94, v18, s2, v14
	v_mov_b32_e32 v95, v105
	v_lshl_add_u64 v[12:13], v[12:13], 0, v[16:17]
	v_lshl_add_u64 v[14:15], s[0:1], 0, v[94:95]
	v_lshl_add_u64 v[14:15], v[14:15], 0, v[16:17]
	global_load_dwordx4 v[86:89], v[12:13], off
	global_load_dwordx4 v[90:93], v[14:15], off
	s_waitcnt vmcnt(15)
	ds_write_b128 v104, v[2:5] offset:57408
	s_waitcnt vmcnt(14)
	ds_write_b128 v104, v[6:9] offset:61504
	v_lshl_add_u64 v[2:3], s[6:7], 0, v[10:11]
	s_waitcnt lgkmcnt(0)
	s_barrier
	global_load_dwordx4 v[34:37], v[2:3], off
	v_lshl_add_u64 v[2:3], s[4:5], 0, v[10:11]
	v_add_u32_e32 v4, 0x3000, v106
	v_mov_b32_e32 v5, v105
	v_lshl_add_u64 v[4:5], v[4:5], 4, s[4:5]
	global_load_dwordx4 v[30:33], v[2:3], off
	global_load_dwordx4 v[26:29], v[4:5], off
	v_add_u32_e32 v2, 0x6000, v106
	v_mov_b32_e32 v3, v105
	v_lshl_add_u64 v[2:3], v[2:3], 4, s[4:5]
	v_add_u32_e32 v4, 0x9000, v106
	v_mov_b32_e32 v5, v105
	v_lshl_add_u64 v[4:5], v[4:5], 4, s[4:5]
	global_load_dwordx4 v[22:25], v[2:3], off
	global_load_dwordx4 v[18:21], v[4:5], off
	v_add_u32_e32 v2, 0xc000, v106
	v_mov_b32_e32 v3, v105
	v_lshl_add_u64 v[2:3], v[2:3], 4, s[4:5]
	v_add_u32_e32 v4, 0xf000, v106
	v_mov_b32_e32 v5, v105
	v_lshl_add_u64 v[4:5], v[4:5], 4, s[4:5]
	global_load_dwordx4 v[14:17], v[2:3], off
	global_load_dwordx4 v[10:13], v[4:5], off
	v_add_u32_e32 v2, 0x12000, v106
	v_mov_b32_e32 v3, v105
	v_lshl_add_u64 v[108:109], v[2:3], 4, s[4:5]
	v_add_u32_e32 v2, 0x15000, v106
	v_lshl_add_u64 v[106:107], v[2:3], 4, s[4:5]
	global_load_dwordx4 v[6:9], v[108:109], off
	global_load_dwordx4 v[2:5], v[106:107], off
	v_bfe_u32 v113, v0, 5, 1
	v_lshrrev_b32_e32 v115, 6, v0
	v_lshlrev_b32_e32 v112, 2, v113
	v_and_b32_e32 v111, 31, v0
	v_or_b32_e32 v116, v112, v115
	v_lshl_or_b32 v120, v116, 5, v111
	v_lshlrev_b32_e32 v108, 4, v120
	ds_read_b32 v140, v108 offset:57420
	ds_read_b32 v141, v108 offset:61516
	ds_read_u16 v158, v108 offset:57408
	ds_read_u16 v159, v108 offset:61504
	v_lshlrev_b32_e32 v142, 9, v116
	v_add_u32_e32 v142, 0x200, v142
	v_add_u32_e32 v143, 0x1000, v142
	v_mov_b32_e32 v152, 0x2000
	s_waitcnt lgkmcnt(0)
	v_cmp_lt_u32_e64 s[28:29], 12, v158
	v_cmp_lt_u32_e64 s[30:31], 12, v159
	v_ffbl_b32_e32 v153, v140
	v_ffbl_b32_e32 v154, v141
	v_cmp_ne_u32_e32 vcc, 0, v140
	v_cmp_ne_u32_e64 s[22:23], 0, v141
	v_lshl_add_u32 v153, v153, 4, v142
	v_lshl_add_u32 v154, v154, 4, v143
	v_cndmask_b32_e32 v144, v152, v153, vcc
	v_cndmask_b32_e64 v148, v152, v154, s[22:23]
	v_add_u32_e32 v153, -1, v140
	v_add_u32_e32 v154, -1, v141
	v_and_b32_e32 v140, v153, v140
	v_and_b32_e32 v141, v154, v141
	v_ffbl_b32_e32 v153, v140
	v_ffbl_b32_e32 v154, v141
	v_cmp_ne_u32_e32 vcc, 0, v140
	v_cmp_ne_u32_e64 s[22:23], 0, v141
	v_lshl_add_u32 v153, v153, 4, v142
	v_lshl_add_u32 v154, v154, 4, v143
	v_cndmask_b32_e32 v145, v152, v153, vcc
	v_cndmask_b32_e64 v149, v152, v154, s[22:23]
	v_add_u32_e32 v153, -1, v140
	v_add_u32_e32 v154, -1, v141
	v_and_b32_e32 v140, v153, v140
	v_and_b32_e32 v141, v154, v141
	v_ffbl_b32_e32 v153, v140
	v_ffbl_b32_e32 v154, v141
	v_cmp_ne_u32_e32 vcc, 0, v140
	v_cmp_ne_u32_e64 s[22:23], 0, v141
	v_lshl_add_u32 v153, v153, 4, v142
	v_lshl_add_u32 v154, v154, 4, v143
	v_cndmask_b32_e32 v146, v152, v153, vcc
	v_cndmask_b32_e64 v150, v152, v154, s[22:23]
	v_add_u32_e32 v153, -1, v140
	v_add_u32_e32 v154, -1, v141
	v_and_b32_e32 v140, v153, v140
	v_and_b32_e32 v141, v154, v141
	v_ffbl_b32_e32 v153, v140
	v_ffbl_b32_e32 v154, v141
	v_cmp_ne_u32_e32 vcc, 0, v140
	v_cmp_ne_u32_e64 s[22:23], 0, v141
	v_lshl_add_u32 v153, v153, 4, v142
	v_lshl_add_u32 v154, v154, 4, v143
	v_cndmask_b32_e32 v147, v152, v153, vcc
	v_cndmask_b32_e64 v151, v152, v154, s[22:23]
	v_add_u32_e32 v153, -1, v140
	v_add_u32_e32 v154, -1, v141
	v_and_b32_e32 v140, v153, v140
	v_and_b32_e32 v141, v154, v141
	v_lshl_or_b32 v144, v145, 16, v144
	v_lshl_or_b32 v145, v147, 16, v146
	v_lshl_or_b32 v148, v149, 16, v148
	v_lshl_or_b32 v149, v151, 16, v150
	v_lshrrev_b32_e32 v153, 1, v108
	v_add_u32_e32 v153, 0x118c0, v153
	v_lshrrev_b32_e32 v154, 2, v108
	v_add_u32_e32 v154, 0x128c0, v154
	ds_write_b64 v153, v[144:145]
	ds_write_b64 v153, v[148:149] offset:2048
	ds_write_b32 v154, v140
	ds_write_b32 v154, v141 offset:1024
	ds_read_b64 v[106:107], v108 offset:57408
	ds_read_u16 v118, v108 offset:57410
	v_and_b32_e32 v114, 63, v0
	v_and_b32_e32 v0, 32, v0
	v_add_u32_e32 v117, 0xe040, v108
	v_mov_b32_e32 v108, -1
	v_mov_b32_e32 v119, v105
	s_branch .LBB2_2

.LBB2_12:
	s_or_b64 exec, exec, s[12:13]
	v_lshlrev_b32_e32 v106, 9, v119
	v_ffbl_b32_e32 v107, v107
	v_ffbl_b32_e32 v108, v108
	v_lshlrev_b32_e32 v116, 25, v119
	v_lshl_or_b32 v107, v107, 4, v106
	v_mov_b32_e32 v109, 0x2000
	v_lshl_or_b32 v108, v108, 20, v116
	v_bfrev_b32_e32 v116, 4
	v_ffbl_b32_e32 v0, v0
	v_cndmask_b32_e64 v107, v107, v109, s[8:9]
	v_cndmask_b32_e64 v108, v108, v116, s[4:5]
	v_lshl_or_b32 v0, v0, 4, v106
	v_cndmask_b32_e32 v0, v0, v109, vcc
	v_or_b32_e32 v106, v108, v107
	v_mov_b32_e32 v108, 0x800000
	v_lshlrev_b32_e32 v107, 16, v117
	v_cndmask_b32_e64 v108, 0, v108, s[6:7]
	s_waitcnt lgkmcnt(2)
	v_lshl_or_b32 v0, v118, 24, v0
	v_or3_b32 v0, v0, v108, v107
	ds_write2_b32 v105, v106, v0 offset0:1 offset1:3
	v_cmp_ne_u32_e32 vcc, 0, v140
	v_cmp_ne_u32_e64 s[22:23], 0, v141
	v_lshlrev_b32_e32 v150, 5, v113
	v_lshl_add_u32 v155, v113, 2, v115
	v_lshlrev_b32_e32 v155, 2, v155
	v_add_u32_e32 v155, 0x11840, v155
	v_lshrrev_b64 v[146:147], v150, vcc
	v_lshrrev_b64 v[156:157], v150, s[22:23]
	v_mov_b32_e32 v151, 0x400
	v_cmp_ne_u32_e32 vcc, 0, v146
	v_cmp_ne_u32_e64 s[22:23], 0, v156
	s_nop 1
	v_cndmask_b32_e32 v146, 0, v151, vcc
	v_cndmask_b32_e64 v156, 0, v151, s[22:23]
	v_lshrrev_b64 v[148:149], v150, s[28:29]
	v_lshrrev_b64 v[152:153], v150, s[30:31]
	v_mov_b32_e32 v154, 0x800
	v_cmp_ne_u32_e32 vcc, 0, v148
	v_cmp_ne_u32_e64 s[22:23], 0, v152
	s_nop 1
	v_cndmask_b32_e32 v148, 0, v154, vcc
	v_cndmask_b32_e64 v152, 0, v154, s[22:23]
	v_or_b32_e32 v146, v146, v148
	v_or_b32_e32 v156, v156, v152
	v_cmp_eq_u32_e32 vcc, 0, v111
	s_and_saveexec_b64 s[22:23], vcc
	ds_or_b32 v155, v146
	ds_or_b32 v155, v156 offset:32
	s_or_b64 exec, exec, s[22:23]
	s_movk_i32 s2, 0x2010
	v_mul_u32_u24_e32 v105, 0x2010, v115
	v_cmp_eq_u32_e32 vcc, 0, v114
	s_waitcnt vmcnt(22)
	ds_write_b128 v104, v[38:41] offset:32832
	s_waitcnt vmcnt(21)
	ds_write_b128 v104, v[42:45] offset:36928
	s_waitcnt vmcnt(20)
	ds_write_b128 v104, v[46:49] offset:41024
	s_waitcnt vmcnt(19)
	ds_write_b128 v104, v[50:53] offset:45120
	s_waitcnt vmcnt(18)
	ds_write_b128 v104, v[54:57] offset:49216
	s_waitcnt vmcnt(17)
	ds_write_b128 v104, v[66:69] offset:53312
	s_and_saveexec_b64 s[0:1], vcc
	v_mov_b32_e32 v38, 0
	v_mov_b32_e32 v39, v38
	v_mov_b32_e32 v40, v38
	v_mov_b32_e32 v41, v38
	ds_write_b128 v105, v[38:41] offset:8192
	s_or_b64 exec, exec, s[0:1]
	v_lshlrev_b32_e32 v40, 3, v113
	v_lshlrev_b32_e32 v67, 4, v110
	v_or_b32_e32 v38, 0x1e0, v111
	v_or_b32_e32 v0, 0x8040, v40
	v_mad_u32_u24 v66, v1, s2, v67
	v_mad_u32_u24 v38, v38, 48, v0
	s_waitcnt vmcnt(16)
	ds_write_b128 v66, v[58:61]
	s_waitcnt vmcnt(15)
	ds_write_b128 v66, v[62:65] offset:1024
	s_waitcnt vmcnt(14)
	ds_write_b128 v66, v[70:73] offset:2048
	s_waitcnt vmcnt(13)
	ds_write_b128 v66, v[74:77] offset:3072
	s_waitcnt vmcnt(12)
	ds_write_b128 v66, v[78:81] offset:4096
	s_waitcnt vmcnt(11)
	ds_write_b128 v66, v[82:85] offset:5120
	s_waitcnt vmcnt(10)
	ds_write_b128 v66, v[86:89] offset:6144
	s_waitcnt vmcnt(9)
	ds_write_b128 v66, v[90:93] offset:7168
	v_lshl_add_u32 v116, v113, 3, v105
	v_or_b32_e32 v106, 0x1e0, v111
	v_lshlrev_b32_e32 v138, 4, v106
	v_lshlrev_b32_e32 v139, 3, v106
	v_add_u32_e32 v139, 0x118c0, v139
	v_mul_u32_u24_e32 v156, 48, v106
	v_add_u32_e32 v156, v0, v156
	v_mov_b32_e32 v157, 0x1187c
	v_add_u32_e32 v137, v116, v138
	v_add_u32_e32 v138, 0x200, v138
	v_lshlrev_b32_e32 v160, 4, v111
	v_lshlrev_b32_e32 v161, 3, v111
	v_add_u32_e32 v161, 0x118c0, v161
	v_mul_u32_u24_e32 v162, 48, v111
	v_add_u32_e32 v162, v0, v162
	v_mov_b32_e32 v163, 0x11840
	v_mul_hi_u32_u24_e32 v159, 0x410, v111
	v_mul_u32_u24_e32 v158, 0x410, v111
	v_mov_b32_e32 v107, 0x82000
	v_mad_u64_u32 v[158:159], s[0:1], s20, v107, v[158:159]
	v_lshlrev_b32_e32 v107, 3, v113
	v_or_b32_e32 v158, v158, v107
	v_lshl_add_u64 v[158:159], s[14:15], 0, v[158:159]
	s_mov_b64 s[0:1], 0x79e30
	s_mov_b32 s2, 0xffff7e00
	s_mov_b32 s3, -1
	v_lshl_add_u64 v[158:159], v[158:159], 0, s[0:1]
	v_lshl_add_u32 v107, v114, 2, v163
	v_add_u32_e32 v107, -8, v107
	s_waitcnt lgkmcnt(0)
	s_barrier
	ds_read_b128 v[38:41], v138 offset:56896
	ds_read_b64 v[42:43], v139
	ds_read2_b64 v[56:59], v156 offset1:2
	ds_read_b32 v60, v107
	v_add_u32_e32 v156, 0xfffffa00, v156
	ds_read2_b64 v[52:55], v156 offset1:2
	v_add_u32_e32 v106, -2, v114
	v_cmp_gt_u32_e32 vcc, 16, v106
	s_waitcnt lgkmcnt(0)
	v_cndmask_b32_e32 v60, 0, v60, vcc
	s_nop 1
	v_readlane_b32 s4, v60, 17
	v_readlane_b32 s21, v60, 16
	v_add_u32_sdwa v92, v105, v56 dst_sel:DWORD dst_unused:UNUSED_PAD src0_sel:DWORD src1_sel:WORD_0
	v_add_u32_sdwa v93, v105, v56 dst_sel:DWORD dst_unused:UNUSED_PAD src0_sel:DWORD src1_sel:WORD_1
	v_add_u32_sdwa v106, v105, v57 dst_sel:DWORD dst_unused:UNUSED_PAD src0_sel:DWORD src1_sel:WORD_0
	v_add_u32_sdwa v107, v105, v57 dst_sel:DWORD dst_unused:UNUSED_PAD src0_sel:DWORD src1_sel:WORD_1
	v_add_u32_sdwa v108, v105, v58 dst_sel:DWORD dst_unused:UNUSED_PAD src0_sel:DWORD src1_sel:WORD_0
	v_add_u32_sdwa v109, v105, v58 dst_sel:DWORD dst_unused:UNUSED_PAD src0_sel:DWORD src1_sel:WORD_1
	ds_read_b128 v[120:123], v92
	ds_read_b128 v[124:127], v93
	ds_read_b128 v[128:131], v106
	ds_read_b128 v[132:135], v107
	ds_read_b128 v[140:143], v108
	ds_read_b128 v[144:147], v109
	v_add_u32_sdwa v88, v116, v42 dst_sel:DWORD dst_unused:UNUSED_PAD src0_sel:DWORD src1_sel:WORD_0
	v_add_u32_sdwa v89, v116, v42 dst_sel:DWORD dst_unused:UNUSED_PAD src0_sel:DWORD src1_sel:WORD_1
	v_add_u32_sdwa v90, v116, v43 dst_sel:DWORD dst_unused:UNUSED_PAD src0_sel:DWORD src1_sel:WORD_0
	v_add_u32_sdwa v91, v116, v43 dst_sel:DWORD dst_unused:UNUSED_PAD src0_sel:DWORD src1_sel:WORD_1
	v_bfe_u32 v117, v41, 16, 7
	v_add_u32_sdwa v118, v116, v39 dst_sel:DWORD dst_unused:UNUSED_PAD src0_sel:DWORD src1_sel:WORD_0
	v_add_u32_sdwa v119, v116, v39 dst_sel:DWORD dst_unused:UNUSED_PAD src0_sel:DWORD src1_sel:WORD_1
	v_add_u32_sdwa v136, v116, v41 dst_sel:DWORD dst_unused:UNUSED_PAD src0_sel:DWORD src1_sel:WORD_0
	s_and_b32 s9, s4, 0xff
	s_waitcnt lgkmcnt(0)
	v_pk_add_f32 v[120:121], v[120:121], v[124:125]
	v_pk_add_f32 v[122:123], v[122:123], v[126:127]
	v_pk_add_f32 v[128:129], v[128:129], v[132:133]
	v_pk_add_f32 v[130:131], v[130:131], v[134:135]
	v_pk_add_f32 v[140:141], v[140:141], v[144:145]
	v_pk_add_f32 v[142:143], v[142:143], v[146:147]
	s_and_b32 s24, s4, 0x900
	s_cbranch_scc1 .Lfarx_pre
.Lfarslow_ret_pre:
	v_pk_add_f32 v[120:121], v[120:121], v[128:129]
	v_pk_add_f32 v[122:123], v[122:123], v[130:131]
	v_pk_add_f32 v[120:121], v[120:121], v[140:141]
	v_pk_add_f32 v[122:123], v[122:123], v[142:143]
	s_nop 1
	v_permlane32_swap_b32_e32 v120, v122
	v_permlane32_swap_b32_e32 v121, v123
	v_pk_add_f32 v[44:45], v[120:121], v[122:123]
	v_add_u32_e32 v138, 0xfffffe00, v138
	v_add_u32_e32 v139, 0xffffff00, v139
	v_add_u32_e32 v156, 0xfffffa00, v156
	v_lshl_add_u64 v[158:159], v[158:159], 0, s[2:3]
	s_mov_b32 s5, 15
	s_mov_b32 s5, 15
.Lit_A:
	ds_read_b64 v[68:69], v88
	ds_read_b64 v[70:71], v89
	ds_read_b64 v[72:73], v90
	ds_read_b64 v[74:75], v91
	v_add_u32_sdwa v92, v105, v52 dst_sel:DWORD dst_unused:UNUSED_PAD src0_sel:DWORD src1_sel:WORD_0
	v_add_u32_sdwa v93, v105, v52 dst_sel:DWORD dst_unused:UNUSED_PAD src0_sel:DWORD src1_sel:WORD_1
	v_add_u32_sdwa v106, v105, v53 dst_sel:DWORD dst_unused:UNUSED_PAD src0_sel:DWORD src1_sel:WORD_0
	v_add_u32_sdwa v107, v105, v53 dst_sel:DWORD dst_unused:UNUSED_PAD src0_sel:DWORD src1_sel:WORD_1
	v_add_u32_sdwa v108, v105, v54 dst_sel:DWORD dst_unused:UNUSED_PAD src0_sel:DWORD src1_sel:WORD_0
	v_add_u32_sdwa v109, v105, v54 dst_sel:DWORD dst_unused:UNUSED_PAD src0_sel:DWORD src1_sel:WORD_1
	ds_read_b128 v[120:123], v92
	ds_read_b128 v[124:127], v93
	ds_read_b128 v[128:131], v106
	ds_read_b128 v[132:135], v107
	ds_read_b128 v[140:143], v108
	ds_read_b128 v[144:147], v109
	s_waitcnt lgkmcnt(6)
	v_pk_add_f32 v[76:77], v[44:45], v[68:69]
	v_pk_add_f32 v[78:79], v[70:71], v[72:73]
	v_pk_add_f32 v[76:77], v[76:77], v[74:75]
	ds_read_b128 v[46:49], v138 offset:56896
	v_pk_add_f32 v[76:77], v[76:77], v[78:79]
	ds_read_b64 v[50:51], v139
	s_bitcmp1_b32 s4, 10
	s_cbranch_scc1 .Lnearslow_A
.Lnearslow_ret_A:
	v_pk_mul_f32 v[78:79], v[40:41], v[76:77] op_sel_hi:[0,1]
	v_cmp_eq_u32_e64 s[6:7], 1, v117
	v_cmp_eq_u32_e64 s[26:27], 2, v117
	ds_write_b64 v137, v[78:79]
	ds_read2_b64 v[56:59], v156 offset1:2
	ds_read_b64 v[82:83], v118
	ds_read_b64 v[84:85], v119
	ds_read_b64 v[86:87], v136
	s_waitcnt lgkmcnt(6)
	v_pk_add_f32 v[120:121], v[120:121], v[124:125]
	v_pk_add_f32 v[122:123], v[122:123], v[126:127]
	v_pk_add_f32 v[128:129], v[128:129], v[132:133]
	v_pk_add_f32 v[130:131], v[130:131], v[134:135]
	v_pk_add_f32 v[140:141], v[140:141], v[144:145]
	v_pk_add_f32 v[142:143], v[142:143], v[146:147]
	s_and_b32 s24, s21, 0x900
	s_cbranch_scc1 .Lfarx_A
.Lfarslow_ret_A:
	v_pk_add_f32 v[120:121], v[120:121], v[128:129]
	v_pk_add_f32 v[122:123], v[122:123], v[130:131]
	v_pk_add_f32 v[120:121], v[120:121], v[140:141]
	v_pk_add_f32 v[122:123], v[122:123], v[142:143]
	v_add_u32_e32 v138, 0xfffffe00, v138
	v_add_u32_e32 v139, 0xffffff00, v139
	v_permlane32_swap_b32_e32 v120, v122
	v_permlane32_swap_b32_e32 v121, v123
	v_pk_add_f32 v[62:63], v[120:121], v[122:123]
	s_bitcmp1_b32 s4, 9
	s_cbranch_scc1 .Lslowlev_A
	s_waitcnt lgkmcnt(0)
	v_pk_fma_f32 v[80:81], v[40:41], v[82:83], v[78:79] op_sel_hi:[0,1,1]
	s_cmp_lt_u32 s9, 2
	v_pk_fma_f32 v[80:81], v[40:41], v[84:85], v[80:81] op_sel_hi:[0,1,1]
	s_mov_b64 exec, s[6:7]
	v_pk_fma_f32 v[80:81], v[40:41], v[86:87], v[80:81] op_sel_hi:[0,1,1]
	ds_write_b64 v137, v[80:81]
	s_mov_b64 exec, -1
	s_cbranch_scc1 .Lnp_A
	ds_read_b64 v[82:83], v118
	ds_read_b64 v[84:85], v119
	ds_read_b64 v[86:87], v136
	v_add_u32_sdwa v88, v116, v50 dst_sel:DWORD dst_unused:UNUSED_PAD src0_sel:DWORD src1_sel:WORD_0
	v_add_u32_sdwa v89, v116, v50 dst_sel:DWORD dst_unused:UNUSED_PAD src0_sel:DWORD src1_sel:WORD_1
	v_add_u32_sdwa v90, v116, v51 dst_sel:DWORD dst_unused:UNUSED_PAD src0_sel:DWORD src1_sel:WORD_0
	v_add_u32_sdwa v91, v116, v51 dst_sel:DWORD dst_unused:UNUSED_PAD src0_sel:DWORD src1_sel:WORD_1
	v_bfe_u32 v168, v49, 16, 7
	v_add_u32_sdwa v169, v116, v47 dst_sel:DWORD dst_unused:UNUSED_PAD src0_sel:DWORD src1_sel:WORD_0
	v_add_u32_sdwa v170, v116, v47 dst_sel:DWORD dst_unused:UNUSED_PAD src0_sel:DWORD src1_sel:WORD_1
	v_add_u32_sdwa v171, v116, v49 dst_sel:DWORD dst_unused:UNUSED_PAD src0_sel:DWORD src1_sel:WORD_0
	v_add_u32_e32 v156, 0xfffffa00, v156
	v_add_u32_e32 v172, 0xfffffe00, v137
	v_readlane_b32 s4, v60, s5
	v_max_i32_e32 v156, v156, v162
	v_lshl_add_u64 v[158:159], v[158:159], 0, s[2:3]
	s_and_b32 s23, s21, 0xff
	s_waitcnt lgkmcnt(0)
	v_pk_fma_f32 v[80:81], v[40:41], v[82:83], v[78:79] op_sel_hi:[0,1,1]
	s_cmp_lt_u32 s9, 3
	v_pk_fma_f32 v[80:81], v[40:41], v[84:85], v[80:81] op_sel_hi:[0,1,1]
	s_mov_b64 exec, s[26:27]
	v_pk_fma_f32 v[80:81], v[40:41], v[86:87], v[80:81] op_sel_hi:[0,1,1]
	ds_write_b64 v137, v[80:81]
	s_mov_b64 exec, -1
	s_cbranch_scc1 .Lbot_A
	s_mov_b32 s8, 3

.Lit_B:
	ds_read_b64 v[68:69], v88
	ds_read_b64 v[70:71], v89
	ds_read_b64 v[72:73], v90
	ds_read_b64 v[74:75], v91
	v_add_u32_sdwa v92, v105, v56 dst_sel:DWORD dst_unused:UNUSED_PAD src0_sel:DWORD src1_sel:WORD_0
	v_add_u32_sdwa v93, v105, v56 dst_sel:DWORD dst_unused:UNUSED_PAD src0_sel:DWORD src1_sel:WORD_1
	v_add_u32_sdwa v106, v105, v57 dst_sel:DWORD dst_unused:UNUSED_PAD src0_sel:DWORD src1_sel:WORD_0
	v_add_u32_sdwa v107, v105, v57 dst_sel:DWORD dst_unused:UNUSED_PAD src0_sel:DWORD src1_sel:WORD_1
	v_add_u32_sdwa v108, v105, v58 dst_sel:DWORD dst_unused:UNUSED_PAD src0_sel:DWORD src1_sel:WORD_0
	v_add_u32_sdwa v109, v105, v58 dst_sel:DWORD dst_unused:UNUSED_PAD src0_sel:DWORD src1_sel:WORD_1
	ds_read_b128 v[120:123], v92
	ds_read_b128 v[124:127], v93
	ds_read_b128 v[128:131], v106
	ds_read_b128 v[132:135], v107
	ds_read_b128 v[140:143], v108
	ds_read_b128 v[144:147], v109
	s_waitcnt lgkmcnt(6)
	v_pk_add_f32 v[76:77], v[62:63], v[68:69]
	v_pk_add_f32 v[78:79], v[70:71], v[72:73]
	v_pk_add_f32 v[76:77], v[76:77], v[74:75]
	ds_read_b128 v[38:41], v138 offset:56896
	v_pk_add_f32 v[76:77], v[76:77], v[78:79]
	ds_read_b64 v[42:43], v139
	s_bitcmp1_b32 s21, 10
	s_cbranch_scc1 .Lnearslow_B
.Lnearslow_ret_B:
	v_pk_mul_f32 v[78:79], v[48:49], v[76:77] op_sel_hi:[0,1]
	v_cmp_eq_u32_e64 s[6:7], 1, v168
	v_cmp_eq_u32_e64 s[26:27], 2, v168
	ds_write_b64 v172, v[78:79]
	ds_read2_b64 v[52:55], v156 offset1:2
	ds_read_b64 v[82:83], v169
	ds_read_b64 v[84:85], v170
	ds_read_b64 v[86:87], v171
	s_waitcnt lgkmcnt(6)
	v_pk_add_f32 v[120:121], v[120:121], v[124:125]
	v_pk_add_f32 v[122:123], v[122:123], v[126:127]
	v_pk_add_f32 v[128:129], v[128:129], v[132:133]
	v_pk_add_f32 v[130:131], v[130:131], v[134:135]
	v_pk_add_f32 v[140:141], v[140:141], v[144:145]
	v_pk_add_f32 v[142:143], v[142:143], v[146:147]
	s_and_b32 s24, s4, 0x900
	s_cbranch_scc1 .Lfarx_B
.Lfarslow_ret_B:
	v_pk_add_f32 v[120:121], v[120:121], v[128:129]
	v_pk_add_f32 v[122:123], v[122:123], v[130:131]
	v_pk_add_f32 v[120:121], v[120:121], v[140:141]
	v_pk_add_f32 v[122:123], v[122:123], v[142:143]
	v_add_u32_e32 v138, 0xfffffe00, v138
	v_add_u32_e32 v139, 0xffffff00, v139
	v_permlane32_swap_b32_e32 v120, v122
	v_permlane32_swap_b32_e32 v121, v123
	v_pk_add_f32 v[44:45], v[120:121], v[122:123]
	s_bitcmp1_b32 s21, 9
	s_cbranch_scc1 .Lslowlev_B
	s_waitcnt lgkmcnt(0)
	v_pk_fma_f32 v[80:81], v[48:49], v[82:83], v[78:79] op_sel_hi:[0,1,1]
	s_cmp_lt_u32 s23, 2
	v_pk_fma_f32 v[80:81], v[48:49], v[84:85], v[80:81] op_sel_hi:[0,1,1]
	s_mov_b64 exec, s[6:7]
	v_pk_fma_f32 v[80:81], v[48:49], v[86:87], v[80:81] op_sel_hi:[0,1,1]
	ds_write_b64 v172, v[80:81]
	s_mov_b64 exec, -1
	s_cbranch_scc1 .Lnp_B
	ds_read_b64 v[82:83], v169
	ds_read_b64 v[84:85], v170
	ds_read_b64 v[86:87], v171
	v_add_u32_sdwa v88, v116, v42 dst_sel:DWORD dst_unused:UNUSED_PAD src0_sel:DWORD src1_sel:WORD_0
	v_add_u32_sdwa v89, v116, v42 dst_sel:DWORD dst_unused:UNUSED_PAD src0_sel:DWORD src1_sel:WORD_1
	v_add_u32_sdwa v90, v116, v43 dst_sel:DWORD dst_unused:UNUSED_PAD src0_sel:DWORD src1_sel:WORD_0
	v_add_u32_sdwa v91, v116, v43 dst_sel:DWORD dst_unused:UNUSED_PAD src0_sel:DWORD src1_sel:WORD_1
	v_bfe_u32 v117, v41, 16, 7
	v_add_u32_sdwa v118, v116, v39 dst_sel:DWORD dst_unused:UNUSED_PAD src0_sel:DWORD src1_sel:WORD_0
	v_add_u32_sdwa v119, v116, v39 dst_sel:DWORD dst_unused:UNUSED_PAD src0_sel:DWORD src1_sel:WORD_1
	v_add_u32_sdwa v136, v116, v41 dst_sel:DWORD dst_unused:UNUSED_PAD src0_sel:DWORD src1_sel:WORD_0
	v_add_u32_e32 v156, 0xfffffa00, v156
	v_add_u32_e32 v137, 0xfffffe00, v172
	v_readlane_b32 s21, v60, s5
	v_max_i32_e32 v156, v156, v162
	v_lshl_add_u64 v[158:159], v[158:159], 0, s[2:3]
	s_and_b32 s9, s4, 0xff
	s_waitcnt lgkmcnt(0)
	v_pk_fma_f32 v[80:81], v[48:49], v[82:83], v[78:79] op_sel_hi:[0,1,1]
	s_cmp_lt_u32 s23, 3
	v_pk_fma_f32 v[80:81], v[48:49], v[84:85], v[80:81] op_sel_hi:[0,1,1]
	s_mov_b64 exec, s[26:27]
	v_pk_fma_f32 v[80:81], v[48:49], v[86:87], v[80:81] op_sel_hi:[0,1,1]
	ds_write_b64 v172, v[80:81]
	s_mov_b64 exec, -1
	s_cbranch_scc1 .Lbot_B
	s_mov_b32 s8, 3

.Lfarx_pre:
	s_waitcnt lgkmcnt(0)
	v_add_u32_sdwa v92, v105, v59 dst_sel:DWORD dst_unused:UNUSED_PAD src0_sel:DWORD src1_sel:WORD_0
	v_add_u32_sdwa v93, v105, v59 dst_sel:DWORD dst_unused:UNUSED_PAD src0_sel:DWORD src1_sel:WORD_1
	ds_read_b128 v[148:151], v92
	ds_read_b128 v[152:155], v93
	s_waitcnt lgkmcnt(0)
	v_pk_add_f32 v[148:149], v[148:149], v[152:153]
	v_pk_add_f32 v[150:151], v[150:151], v[154:155]
	v_pk_add_f32 v[140:141], v[140:141], v[148:149]
	v_pk_add_f32 v[142:143], v[142:143], v[150:151]
	s_bitcmp1_b32 s4, 8
	s_cbranch_scc0 .Lfarslow_ret_pre
	s_branch .Lfarslow_pre
.Lfarx_A:
	s_waitcnt lgkmcnt(0)
	v_add_u32_sdwa v92, v105, v55 dst_sel:DWORD dst_unused:UNUSED_PAD src0_sel:DWORD src1_sel:WORD_0
	v_add_u32_sdwa v93, v105, v55 dst_sel:DWORD dst_unused:UNUSED_PAD src0_sel:DWORD src1_sel:WORD_1
	ds_read_b128 v[148:151], v92
	ds_read_b128 v[152:155], v93
	s_waitcnt lgkmcnt(0)
	v_pk_add_f32 v[148:149], v[148:149], v[152:153]
	v_pk_add_f32 v[150:151], v[150:151], v[154:155]
	v_pk_add_f32 v[140:141], v[140:141], v[148:149]
	v_pk_add_f32 v[142:143], v[142:143], v[150:151]
	s_bitcmp1_b32 s21, 8
	s_cbranch_scc0 .Lfarslow_ret_A
	s_branch .Lfarslow_A

.Lfs_gather_pre:
	v_add_u32_sdwa v92, v105, v64 dst_sel:DWORD dst_unused:UNUSED_PAD src0_sel:DWORD src1_sel:WORD_0
	v_add_u32_sdwa v93, v105, v64 dst_sel:DWORD dst_unused:UNUSED_PAD src0_sel:DWORD src1_sel:WORD_1
	v_add_u32_sdwa v106, v105, v65 dst_sel:DWORD dst_unused:UNUSED_PAD src0_sel:DWORD src1_sel:WORD_0
	v_add_u32_sdwa v107, v105, v65 dst_sel:DWORD dst_unused:UNUSED_PAD src0_sel:DWORD src1_sel:WORD_1
	ds_read_b128 v[124:127], v92
	ds_read_b128 v[132:135], v93
	ds_read_b128 v[144:147], v106
	ds_read_b128 v[152:155], v107
	s_waitcnt lgkmcnt(0)
	v_pk_add_f32 v[124:125], v[124:125], v[132:133]
	v_pk_add_f32 v[126:127], v[126:127], v[134:135]
	v_pk_add_f32 v[144:145], v[144:145], v[152:153]
	v_pk_add_f32 v[146:147], v[146:147], v[154:155]
	v_pk_add_f32 v[124:125], v[124:125], v[144:145]
	v_pk_add_f32 v[126:127], v[126:127], v[146:147]
	s_nop 0
	v_pk_add_f32 v[140:141], v[140:141], v[124:125]
	v_pk_add_f32 v[142:143], v[142:143], v[126:127]
	v_cmp_lt_u32_e32 vcc, s22, v164
	s_cbranch_vccz .Lfarslow_ret_pre
	v_add_u32_e32 v165, s22, v112
	v_cmp_lt_u32_e32 vcc, v165, v164
	v_mov_b32_e32 v64, 0x20002000
	v_mov_b32_e32 v65, 0x20002000
	s_and_saveexec_b64 s[12:13], vcc
	global_load_dwordx2 v[64:65], v[166:167], off
	s_mov_b64 exec, -1
	v_lshl_add_u64 v[166:167], v[166:167], 0, 16
	s_add_i32 s22, s22, 8
	s_waitcnt vmcnt(0)
	s_branch .Lfs_gather_pre
